# schedule: weight-conversion split moved 840 blocks per layer from the in_proj spare workgroups into the mixer phase (its marginal cost there measured near zero)
# baseline (speedup 1.0000x reference)
.LBB0_310:
	s_lshl_b32 s4, s2, 3
	v_writelane_b32 v254, s4, 7
	s_lshl_b32 s4, s3, 3
	v_writelane_b32 v254, s4, 8
	s_lshl_b32 s4, s2, 9
	s_lshl_b32 s62, s3, 9
	s_cmp_eq_u32 s2, 0
	v_writelane_b32 v254, s4, 9
	s_cselect_b64 s[4:5], -1, 0
	v_writelane_b32 v254, s4, 10
	s_lshl_b32 s8, s2, 5
	s_and_b32 s14, s87, 31
	v_writelane_b32 v254, s5, 11
	s_mul_i32 s4, s2, 0x6b
	s_add_i32 s7, s4, 0xffffd954
	s_ashr_i32 s11, s87, 5
	s_lshl_b32 s4, s2, 4
	s_lshl_b32 s66, s3, 4
	s_cmpk_lt_i32 s2, 0x100
	v_writelane_b32 v254, s4, 12
	s_cselect_b64 s[4:5], -1, 0
	v_writelane_b32 v254, s4, 13
	s_movk_i32 s64, 0x80
	s_movk_i32 s65, 0xff00
	v_writelane_b32 v254, s5, 14
	s_lshr_b32 s4, s2, 3
	s_mul_i32 s4, s4, 5
	s_and_b32 s5, s2, 7
	s_add_i32 s4, s4, s5
	s_add_i32 s4, s4, -3
	s_cmp_lt_u32 s5, 3
	s_cselect_b32 s4, 0x7fff, s4
	s_cmpk_lt_i32 s4, 0x80
	v_writelane_b32 v254, s4, 15
	s_cselect_b64 s[4:5], -1, 0
	s_and_b32 s9, s87, 3
	v_writelane_b32 v254, s4, 16
	s_cmpk_lt_i32 s2, 0x200
	s_movk_i32 s56, 0x1000
	v_writelane_b32 v254, s5, 17
	s_cselect_b64 s[4:5], -1, 0
	v_writelane_b32 v254, s4, 18
	s_lshl_b32 s74, s3, 5
	s_movk_i32 s77, 0x4400
	v_writelane_b32 v254, s5, 19
	s_lshl_b32 s4, s2, 2
	s_and_b32 s4, s4, 0xffffff00
	v_writelane_b32 v254, s4, 20
	s_lshl_b32 s4, s2, 6
	s_and_b32 s6, s4, 0xfc0
	s_cmp_gt_i32 s3, 0
	v_writelane_b32 v254, s4, 21
	s_cselect_b64 s[4:5], -1, 0
	v_writelane_b32 v254, s4, 22
	s_ashr_i32 s12, s87, 2
	s_mov_b32 s10, s12
	v_writelane_b32 v254, s5, 23
	s_ashr_i32 s4, s87, 3
	v_writelane_b32 v254, s4, 24
	s_and_b32 s5, s87, 7
	s_lshl_b32 s4, s5, 7
	v_writelane_b32 v254, s5, 25
	s_lshl_b32 s5, s5, 18
	v_writelane_b32 v254, s5, 26
	s_ashr_i32 s13, s12, 31
	v_writelane_b32 v254, s10, 27
	s_lshl_b64 s[12:13], s[12:13], 18
	s_lshl_b32 s5, s9, 8
	v_writelane_b32 v254, s11, 28
	v_writelane_b32 v254, s12, 29
	s_mov_b32 s38, 0x78787879
	s_movk_i32 s39, 0xef00
	v_writelane_b32 v254, s13, 30
	v_writelane_b32 v254, s9, 31
	s_lshl_b32 s9, s9, 18
	s_cmpk_lt_i32 s2, 0x84
	v_writelane_b32 v254, s9, 32
	s_cselect_b32 s9, 32, 0x6b
	v_writelane_b32 v254, s9, 33
	v_writelane_b32 v254, s8, 34
	s_cselect_b32 s7, s8, s7
	v_writelane_b32 v254, s7, 35
	s_add_i32 s7, s3, -1
	s_cmp_gt_u32 s7, 6
	s_cselect_b64 s[8:9], -1, 0
	s_abs_i32 s12, s3
	v_cvt_f32_u32_e32 v1, s12
	v_writelane_b32 v254, s8, 36
	s_sub_i32 s7, 0, s12
	s_and_b32 s76, s3, 0x7ffffff8
	v_rcp_iflag_f32_e32 v1, v1
	v_writelane_b32 v254, s9, 37
	s_ashr_i32 s13, s3, 31
	s_mov_b32 s59, 0x800000
	v_mul_f32_e32 v1, 0x4f7ffffe, v1
	v_cvt_u32_f32_e32 v1, v1
	v_mov_b32_e32 v205, 1
	v_mov_b32_e32 v221, 0x1400
	v_mov_b32_e32 v204, 0x20200
	v_readfirstlane_b32 s8, v1
	s_mul_i32 s7, s7, s8
	s_mul_hi_u32 s7, s8, s7
	s_add_i32 s7, s8, s7
	v_writelane_b32 v254, s7, 38
	s_mul_hi_u32 s7, s7, 0xa1b
	s_mul_i32 s8, s7, s12
	s_sub_i32 s8, 0xa1b, s8
	s_add_i32 s9, s7, 1
	s_sub_i32 s10, s8, s12
	s_cmp_ge_u32 s8, s12
	s_cselect_b32 s7, s9, s7
	s_cselect_b32 s8, s10, s8
	s_add_i32 s9, s7, 1
	s_cmp_ge_u32 s8, s12
	s_cselect_b32 s7, s9, s7
	s_xor_b32 s7, s7, s13
	s_sub_i32 s7, s7, s13
	s_mul_i32 s8, s7, s3
	s_sub_i32 s8, 0xa1b, s8
	s_mul_i32 s9, s7, s87
	s_min_i32 s10, s87, s8
	v_writelane_b32 v254, s12, 39
	s_add_i32 s9, s9, s10
	v_writelane_b32 v254, s13, 40
	s_cmp_lt_i32 s87, s8
	v_writelane_b32 v254, s9, 41
	s_cselect_b64 s[8:9], -1, 0
	s_cmp_lg_u64 s[8:9], 0
	s_addc_u32 s7, s7, 0
	v_writelane_b32 v254, s7, 42
	s_lshl_b32 s7, s3, 1
	v_writelane_b32 v254, s7, 43
	s_add_i32 s7, s11, 17
	v_writelane_b32 v254, s7, 44
	s_lshl_b32 s7, s7, 4
	v_writelane_b32 v254, s7, 45
	s_lshl_b32 s7, s14, 4
	v_writelane_b32 v254, s14, 46
	s_add_i32 s8, s7, 0xd250
	v_writelane_b32 v254, s8, 47
	s_add_i32 s8, s11, 9
	v_writelane_b32 v254, s8, 48
	s_lshl_b32 s8, s8, 4
	v_writelane_b32 v254, s8, 49
	v_writelane_b32 v254, s11, 50
	s_add_i32 s8, s11, 1
	v_writelane_b32 v254, s8, 51
	s_or_b32 s8, s7, 0xfffffe00
	v_writelane_b32 v254, s8, 52
	s_lshl_b32 s8, s3, 6
	v_writelane_b32 v254, s8, 53
	s_add_i32 s7, s7, 0xa050
	v_writelane_b32 v254, s7, 54
	s_add_i32 s7, 0, 0x12000
	v_writelane_b32 v254, s7, 55
	s_add_i32 s7, 0, 0x27020
	v_writelane_b32 v254, s7, 56
	s_add_i32 s7, 0, 0x27024
	v_writelane_b32 v254, s7, 57
	s_add_i32 s7, 0, 0x25000
	v_writelane_b32 v254, s7, 58
	s_lshl_b32 s6, s6, 1
	v_writelane_b32 v254, s6, 59
	s_lshl_b32 s5, s5, 2
	v_writelane_b32 v254, s5, 60
	s_add_i32 s5, 0, 0x25400
	v_writelane_b32 v254, s5, 61
	s_add_i32 s5, 0, 0x10200
	v_writelane_b32 v254, s5, 62
	s_add_i32 s5, 0, 0x20100
	v_writelane_b32 v254, s5, 63
	s_add_i32 s5, 0, 0x20010
	v_writelane_b32 v255, s5, 0
	s_add_i32 s5, 0, 0x20110
	v_writelane_b32 v255, s5, 1
	s_add_i32 s5, 0, 0x20020
	v_writelane_b32 v255, s5, 2
	s_add_i32 s5, 0, 0x20120
	v_writelane_b32 v255, s5, 3
	s_add_i32 s5, 0, 0x20030
	v_writelane_b32 v255, s5, 4
	s_add_i32 s5, 0, 0x20130
	v_writelane_b32 v255, s5, 5
	s_add_i32 s5, 0, 0x20040
	v_writelane_b32 v255, s5, 6
	s_add_i32 s5, 0, 0x20140
	v_writelane_b32 v255, s5, 7
	s_add_i32 s5, 0, 0x20050
	v_writelane_b32 v255, s5, 8
	s_add_i32 s5, 0, 0x20150
	v_writelane_b32 v255, s5, 9
	s_add_i32 s5, 0, 0x20060
	v_writelane_b32 v255, s5, 10
	s_add_i32 s5, 0, 0x20160
	v_writelane_b32 v255, s5, 11
	s_add_i32 s5, 0, 0x20070
	v_writelane_b32 v255, s5, 12
	s_add_i32 s5, 0, 0x20170
	v_writelane_b32 v255, s5, 13
	s_add_i32 s5, 0, 0x20180
	v_writelane_b32 v255, s5, 14
	s_add_i32 s5, 0, 0x20084
	v_writelane_b32 v255, s5, 15
	s_add_i32 s5, 0, 0x20024
	v_writelane_b32 v255, s5, 16
	s_add_i32 s5, 0, 0x2002c
	v_writelane_b32 v255, s5, 17
	s_add_i32 s5, 0, 0x20034
	v_writelane_b32 v255, s5, 18
	s_add_i32 s5, 0, 0x2003c
	v_writelane_b32 v255, s5, 19
	s_add_i32 s5, 0, 0x20044
	v_writelane_b32 v255, s5, 20
	s_add_i32 s5, 0, 0x2004c
	v_writelane_b32 v255, s5, 21
	s_add_i32 s5, 0, 0x20054
	v_writelane_b32 v255, s5, 22
	s_add_i32 s5, 0, 0x2005c
	v_writelane_b32 v255, s5, 23
	s_add_i32 s5, 0, 0x20064
	v_writelane_b32 v255, s5, 24
	s_add_i32 s5, 0, 0x2006c
	v_writelane_b32 v255, s5, 25
	s_add_i32 s5, 0, 0x20074
	v_writelane_b32 v255, s5, 26
	s_add_i32 s5, 0, 0x2007c
	v_writelane_b32 v255, s5, 27
	s_add_i32 s5, 0, 0x20800
	v_writelane_b32 v255, s5, 28
	s_lshl_b32 s4, s4, 2
	v_writelane_b32 v255, s4, 29
	s_ashr_i32 s63, s62, 31
	s_ashr_i32 s67, s66, 31
	v_writelane_b32 v255, s5, 30
	v_cmp_eq_u32_e64 s[4:5], 0, v0
	s_mov_b32 s6, s74
	s_add_i32 s84, 0, 0x20004
	v_writelane_b32 v255, s4, 31
	s_add_i32 s69, 0, 0x2000c
	s_add_i32 s68, 0, 0x20014
	v_writelane_b32 v255, s5, 32
	s_lshl_b64 s[4:5], s[62:63], 2
	v_writelane_b32 v255, s4, 33
	s_add_i32 s49, 0, 0x2001c
	v_mov_b32_e32 v1, 0
	v_writelane_b32 v255, s5, 34
	s_lshl_b64 s[4:5], s[66:67], 12
	v_writelane_b32 v255, s4, 35
	v_mov_b32_e32 v220, 0xff800000
	s_movk_i32 s47, 0x3ff
	v_writelane_b32 v255, s5, 36
	v_writelane_b32 v255, s6, 37
	s_mov_b32 s83, 0x34400000
	s_mov_b32 s80, 0x36500000
	v_writelane_b32 v255, s7, 38
	s_mov_b32 s6, s62
	v_writelane_b32 v255, s6, 39
	s_movk_i32 s81, 0x7fff
	s_mov_b32 s57, 0x41000000
	v_writelane_b32 v255, s7, 40
	s_mov_b32 s6, s66
	v_writelane_b32 v255, s6, 41
	s_movk_i32 s33, 0xfefe
	s_mov_b32 s85, 0x900000
	v_writelane_b32 v255, s7, 42
	v_writelane_b32 v255, s76, 43
	v_writelane_b32 v255, s84, 44
	s_mov_b32 s72, 0xc0e00000
	s_mov_b32 s73, 0
	s_mov_b32 s71, 0
	s_mov_b64 s[4:5], -1
	s_mov_b64 s[78:79], 0x80
	s_mov_b32 s82, 0x3e38aa3b
	s_mov_b32 s88, 0xc01d265f
	s_mov_b32 s50, s69
	s_mov_b32 s86, s68
	s_mov_b32 s60, s49
	v_writelane_b32 v255, s87, 45
	s_branch .LBB0_314

.LBB0_561:
	s_and_b64 vcc, exec, s[16:17]
	s_cbranch_vccz .LBB0_711
	v_readlane_b32 s6, v254, 50
	v_readlane_b32 s7, v254, 46
	s_mul_i32 s6, s35, s6
	s_sub_i32 s7, s7, s36
	s_add_i32 s23, s7, s6
	s_lshl_b32 s22, s35, 3
	s_mov_b64 s[6:7], -1
	s_and_b64 vcc, exec, s[90:91]
	s_cbranch_vccz .LBB0_637
	v_mbcnt_lo_u32_b32 v66, -1, 0
	v_mbcnt_hi_u32_b32 v66, -1, v66
	s_getreg_b32 s6, hwreg(HW_REG_HW_ID, 0, 6)
	s_lshl_b32 s6, s6, 2
	s_and_b32 s6, s6, 0xfc
	s_or_b32 s6, s6, 0x27100
	v_mov_b32_e32 v0, s6
	ds_read_b32 v0, v0
	s_cmpk_gt_i32 s23, 0x9f
	s_waitcnt lgkmcnt(0)
	v_readfirstlane_b32 s9, v0
	s_cbranch_scc1 .LBB0_636
	s_add_i32 s20, s23, 0xd45
	s_mul_hi_i32 s6, s20, 0x2aaaaaab
	s_lshr_b32 s7, s6, 31
	s_ashr_i32 s15, s6, 9
	s_add_i32 s15, s15, s7
	s_mul_i32 s16, s15, 0xfffff400
	s_add_i32 s16, s16, s20
	s_cmpk_gt_i32 s16, 0x7ff
	s_mov_b64 s[12:13], -1
	s_cbranch_scc0 .LBB0_566
	s_add_i32 s6, s16, 0xfffff800
	s_mov_b32 s10, 31
	s_lshl_b32 s7, s15, 5
	s_lshr_b32 s6, s6, 5
	s_lshl_b32 s24, s20, 8
	s_ashr_i32 s11, s10, 31
	s_add_i32 s6, s6, s7
	s_lshl_b32 s14, s20, 5
	s_and_b32 s8, s24, 0x300
	s_lshl_b64 s[10:11], s[10:11], 3
	s_add_u32 s10, s0, s10
	s_addc_u32 s11, s1, s11
	s_load_dwordx2 s[10:11], s[10:11], 0x0
	s_ashr_i32 s7, s6, 31
	s_lshl_b64 s[12:13], s[6:7], 20
	s_lshl_b64 s[6:7], s[6:7], 22
	s_waitcnt lgkmcnt(0)
	s_add_u32 s6, s10, s6
	s_mov_b32 s10, 35
	s_addc_u32 s7, s11, s7
	s_ashr_i32 s11, s10, 31
	s_lshl_b64 s[10:11], s[10:11], 3
	s_add_u32 s10, s0, s10
	s_addc_u32 s11, s1, s11
	s_load_dwordx2 s[10:11], s[10:11], 0x0
	s_waitcnt lgkmcnt(0)
	s_add_u32 s10, s10, s12
	s_addc_u32 s11, s11, s13
	s_add_u32 s10, s10, 0x12800000
	s_addc_u32 s11, s11, 0
	s_mov_b64 s[12:13], 0

.LBB0_571:
	v_ashrrev_i32_e32 v139, 31, v138
	v_lshlrev_b64 v[138:139], 10, v[138:139]
	s_add_i32 s30, s30, s27
	v_readlane_b32 s6, v254, 46
	v_lshl_add_u64 v[138:139], s[16:17], 0, v[138:139]
	s_add_i32 s24, s24, s25
	s_add_i32 s26, s26, s27
	s_add_i32 s36, s36, s28
	s_add_i32 s29, s29, s27
	s_add_i32 s6, s6, s30
	v_lshl_add_u64 v[138:139], v[138:139], 0, s[14:15]
	s_cmpk_gt_i32 s6, 0xde4
	v_lshl_add_u64 v[138:139], v[138:139], 0, v[136:137]
	s_cselect_b64 s[6:7], -1, 0
	s_waitcnt lgkmcnt(0)
	global_store_dwordx4 v[138:139], v[130:133], off nt

.LBB0_573:
	v_readlane_b32 s6, v254, 46
	s_add_i32 s6, s6, s29
	s_add_i32 s9, s20, s22
	s_add_i32 s7, s6, 0xd25
	s_cmpk_lt_i32 s7, 0xde5
	s_cselect_b64 s[18:19], -1, 0
	s_cmpk_gt_i32 s7, 0xde4
	s_cbranch_scc1 .LBB0_580
	s_mul_hi_i32 s7, s7, 0x2aaaaaab
	s_lshr_b32 s12, s7, 31
	s_ashr_i32 s20, s7, 9
	s_add_i32 s20, s20, s12
	s_mul_i32 s7, s20, 0xfffff400
	s_add_i32 s37, s6, s7
	s_add_i32 s21, s37, 0xd25
	s_cmpk_gt_i32 s21, 0x7ff
	s_mov_b64 s[14:15], -1
	s_cbranch_scc0 .LBB0_576
	s_addk_i32 s37, 0x525
	s_mov_b32 s14, 31
	s_lshl_b32 s6, s20, 5
	s_lshr_b32 s7, s37, 5
	s_ashr_i32 s15, s14, 31
	s_add_i32 s6, s7, s6
	s_lshl_b32 s13, s9, 5
	s_and_b32 s12, s24, 0x300
	s_lshl_b64 s[14:15], s[14:15], 3
	s_add_u32 s14, s0, s14
	s_addc_u32 s15, s1, s15
	s_load_dwordx2 s[14:15], s[14:15], 0x0
	s_ashr_i32 s7, s6, 31
	s_lshl_b64 s[16:17], s[6:7], 20
	s_lshl_b64 s[6:7], s[6:7], 22
	s_waitcnt lgkmcnt(0)
	s_add_u32 s6, s14, s6
	s_mov_b32 s14, 35
	s_addc_u32 s7, s15, s7
	s_ashr_i32 s15, s14, 31
	s_lshl_b64 s[14:15], s[14:15], 3
	s_add_u32 s14, s0, s14
	s_addc_u32 s15, s1, s15
	s_load_dwordx2 s[14:15], s[14:15], 0x0
	s_waitcnt lgkmcnt(0)
	s_add_u32 s14, s14, s16
	s_addc_u32 s15, s15, s17
	s_add_u32 s16, s14, 0x12800000
	s_addc_u32 s17, s15, 0
	s_mov_b64 s[14:15], 0

.LBB0_604:
	v_ashrrev_i32_e32 v139, 31, v138
	v_lshlrev_b64 v[138:139], 10, v[138:139]
	v_lshl_add_u64 v[138:139], s[10:11], 0, v[138:139]
	v_lshl_add_u64 v[138:139], v[138:139], 0, s[70:71]
	v_lshl_add_u64 v[138:139], v[138:139], 0, v[136:137]
	s_andn2_b64 vcc, exec, s[18:19]
	s_mov_b64 s[6:7], -1
	s_waitcnt lgkmcnt(0)
	global_store_dwordx4 v[138:139], v[130:133], off nt
	s_cbranch_vccnz .LBB0_572
	v_readlane_b32 s6, v254, 46
	s_add_i32 s6, s6, s26
	s_add_i32 s20, s9, s22
	s_add_i32 s7, s6, 0xd25
	s_cmpk_gt_i32 s7, 0xde4
	s_cbranch_scc1 .LBB0_612
	s_mul_hi_i32 s7, s7, 0x2aaaaaab
	s_lshr_b32 s8, s7, 31
	s_ashr_i32 s13, s7, 9
	s_add_i32 s13, s13, s8
	s_mul_i32 s7, s13, 0xfffff400
	s_add_i32 s21, s6, s7
	s_add_i32 s15, s21, 0xd25
	s_cmpk_gt_i32 s15, 0x7ff
	s_mov_b64 s[18:19], -1
	s_cbranch_scc0 .LBB0_608
	s_addk_i32 s21, 0x525
	s_mov_b32 s10, 31
	s_lshl_b32 s6, s13, 5
	s_lshr_b32 s7, s21, 5
	s_ashr_i32 s11, s10, 31
	s_add_i32 s6, s7, s6
	s_lshl_b32 s9, s20, 5
	s_and_b32 s8, s24, 0x300
	s_lshl_b64 s[10:11], s[10:11], 3
	s_add_u32 s10, s0, s10
	s_addc_u32 s11, s1, s11
	s_load_dwordx2 s[10:11], s[10:11], 0x0
	s_ashr_i32 s7, s6, 31
	s_lshl_b64 s[18:19], s[6:7], 20
	s_lshl_b64 s[6:7], s[6:7], 22
	s_waitcnt lgkmcnt(0)
	s_add_u32 s6, s10, s6
	s_mov_b32 s10, 35
	s_addc_u32 s7, s11, s7
	s_ashr_i32 s11, s10, 31
	s_lshl_b64 s[10:11], s[10:11], 3
	s_add_u32 s10, s0, s10
	s_addc_u32 s11, s1, s11
	s_load_dwordx2 s[10:11], s[10:11], 0x0
	s_waitcnt lgkmcnt(0)
	s_add_u32 s10, s10, s18
	s_addc_u32 s11, s11, s19
	s_add_u32 s10, s10, 0x12800000
	s_addc_u32 s11, s11, 0
	s_mov_b64 s[18:19], 0

.LBB0_637:
	s_andn2_b64 vcc, exec, s[6:7]
	s_cbranch_vccnz .LBB0_711
	v_mbcnt_lo_u32_b32 v66, -1, 0
	v_mbcnt_hi_u32_b32 v66, -1, v66
	s_getreg_b32 s6, hwreg(HW_REG_HW_ID, 0, 6)
	s_lshl_b32 s6, s6, 2
	s_and_b32 s6, s6, 0xfc
	s_or_b32 s6, s6, 0x27100
	v_mov_b32_e32 v0, s6
	ds_read_b32 v0, v0
	s_cmpk_gt_i32 s23, 0x9
	s_waitcnt lgkmcnt(0)
	v_readfirstlane_b32 s9, v0
	s_cbranch_scc1 .LBB0_711
	s_mul_hi_i32 s6, s23, 0x2aaaaaab
	s_lshr_b32 s7, s6, 31
	s_ashr_i32 s15, s6, 9
	s_add_i32 s15, s15, s7
	s_mul_i32 s16, s15, 0xfffff400
	s_add_i32 s16, s16, s23
	s_cmpk_gt_i32 s16, 0x7ff
	s_mov_b64 s[12:13], -1
	s_cbranch_scc0 .LBB0_641
	s_add_i32 s6, s16, 0xfffff800
	s_mov_b32 s10, 31
	s_lshl_b32 s7, s15, 5
	s_lshr_b32 s6, s6, 5
	s_lshl_b32 s24, s23, 8
	s_ashr_i32 s11, s10, 31
	s_add_i32 s6, s6, s7
	s_lshl_b32 s14, s23, 5
	s_and_b32 s8, s24, 0x300
	s_lshl_b64 s[10:11], s[10:11], 3
	s_add_u32 s10, s0, s10
	s_addc_u32 s11, s1, s11
	s_load_dwordx2 s[10:11], s[10:11], 0x0
	s_ashr_i32 s7, s6, 31
	s_lshl_b64 s[12:13], s[6:7], 20
	s_lshl_b64 s[6:7], s[6:7], 22
	s_waitcnt lgkmcnt(0)
	s_add_u32 s6, s10, s6
	s_mov_b32 s10, 35
	s_addc_u32 s7, s11, s7
	s_ashr_i32 s11, s10, 31
	s_lshl_b64 s[10:11], s[10:11], 3
	s_add_u32 s10, s0, s10
	s_addc_u32 s11, s1, s11
	s_load_dwordx2 s[10:11], s[10:11], 0x0
	s_waitcnt lgkmcnt(0)
	s_add_u32 s10, s10, s12
	s_addc_u32 s11, s11, s13
	s_add_u32 s10, s10, 0x12800000
	s_addc_u32 s11, s11, 0
	s_mov_b64 s[12:13], 0

.LBB0_646:
	v_ashrrev_i32_e32 v139, 31, v138
	v_lshlrev_b64 v[138:139], 10, v[138:139]
	s_add_i32 s35, s35, s27
	v_readlane_b32 s6, v254, 46
	v_lshl_add_u64 v[138:139], s[16:17], 0, v[138:139]
	s_add_i32 s24, s24, s25
	s_add_i32 s26, s26, s27
	s_add_i32 s37, s37, s29
	s_add_i32 s30, s30, s27
	s_add_i32 s6, s6, s35
	v_lshl_add_u64 v[138:139], v[138:139], 0, s[14:15]
	s_cmpk_gt_i32 s6, 0x9
	v_lshl_add_u64 v[138:139], v[138:139], 0, v[136:137]
	s_cselect_b64 s[6:7], -1, 0
	s_waitcnt lgkmcnt(0)
	global_store_dwordx4 v[138:139], v[130:133], off nt

.LBB0_648:
	v_readlane_b32 s6, v254, 46
	s_add_i32 s6, s6, s30
	s_add_i32 s9, s23, s22
	s_sub_i32 s7, s6, 32
	s_cmpk_lt_i32 s7, 0xa
	s_cselect_b64 s[18:19], -1, 0
	s_cmpk_gt_i32 s7, 0x9
	s_cbranch_scc1 .LBB0_655
	s_mul_hi_i32 s7, s7, 0x2aaaaaab
	s_lshr_b32 s12, s7, 31
	s_ashr_i32 s20, s7, 9
	s_add_i32 s20, s20, s12
	s_mul_i32 s7, s20, 0xfffff400
	s_add_i32 s23, s6, s7
	s_sub_i32 s21, s23, 32
	s_cmpk_gt_i32 s21, 0x7ff
	s_mov_b64 s[14:15], -1
	s_cbranch_scc0 .LBB0_651
	s_addk_i32 s23, 0xf7e0
	s_mov_b32 s14, 31
	s_lshl_b32 s6, s20, 5
	s_lshr_b32 s7, s23, 5
	s_ashr_i32 s15, s14, 31
	s_add_i32 s6, s7, s6
	s_lshl_b32 s13, s9, 5
	s_and_b32 s12, s24, 0x300
	s_lshl_b64 s[14:15], s[14:15], 3
	s_add_u32 s14, s0, s14
	s_addc_u32 s15, s1, s15
	s_load_dwordx2 s[14:15], s[14:15], 0x0
	s_ashr_i32 s7, s6, 31
	s_lshl_b64 s[16:17], s[6:7], 20
	s_lshl_b64 s[6:7], s[6:7], 22
	s_waitcnt lgkmcnt(0)
	s_add_u32 s6, s14, s6
	s_mov_b32 s14, 35
	s_addc_u32 s7, s15, s7
	s_ashr_i32 s15, s14, 31
	s_lshl_b64 s[14:15], s[14:15], 3
	s_add_u32 s14, s0, s14
	s_addc_u32 s15, s1, s15
	s_load_dwordx2 s[14:15], s[14:15], 0x0
	s_waitcnt lgkmcnt(0)
	s_add_u32 s14, s14, s16
	s_addc_u32 s15, s15, s17
	s_add_u32 s16, s14, 0x12800000
	s_addc_u32 s17, s15, 0
	s_mov_b64 s[14:15], 0

.LBB0_679:
	v_ashrrev_i32_e32 v139, 31, v138
	v_lshlrev_b64 v[138:139], 10, v[138:139]
	v_lshl_add_u64 v[138:139], s[10:11], 0, v[138:139]
	v_lshl_add_u64 v[138:139], v[138:139], 0, s[70:71]
	v_lshl_add_u64 v[138:139], v[138:139], 0, v[136:137]
	s_andn2_b64 vcc, exec, s[18:19]
	s_mov_b64 s[6:7], -1
	s_waitcnt lgkmcnt(0)
	global_store_dwordx4 v[138:139], v[130:133], off nt
	s_cbranch_vccnz .LBB0_647
	v_readlane_b32 s6, v254, 46
	s_add_i32 s6, s6, s26
	s_add_i32 s23, s9, s22
	s_sub_i32 s7, s6, 32
	s_cmpk_gt_i32 s7, 0x9
	s_cbranch_scc1 .LBB0_687
	s_mul_hi_i32 s7, s7, 0x2aaaaaab
	s_lshr_b32 s8, s7, 31
	s_ashr_i32 s13, s7, 9
	s_add_i32 s13, s13, s8
	s_mul_i32 s7, s13, 0xfffff400
	s_add_i32 s20, s6, s7
	s_sub_i32 s15, s20, 32
	s_cmpk_gt_i32 s15, 0x7ff
	s_mov_b64 s[18:19], -1
	s_cbranch_scc0 .LBB0_683
	s_addk_i32 s20, 0xf7e0
	s_mov_b32 s10, 31
	s_lshl_b32 s6, s13, 5
	s_lshr_b32 s7, s20, 5
	s_ashr_i32 s11, s10, 31
	s_add_i32 s6, s7, s6
	s_lshl_b32 s9, s23, 5
	s_and_b32 s8, s24, 0x300
	s_lshl_b64 s[10:11], s[10:11], 3
	s_add_u32 s10, s0, s10
	s_addc_u32 s11, s1, s11
	s_load_dwordx2 s[10:11], s[10:11], 0x0
	s_ashr_i32 s7, s6, 31
	s_lshl_b64 s[18:19], s[6:7], 20
	s_lshl_b64 s[6:7], s[6:7], 22
	s_waitcnt lgkmcnt(0)
	s_add_u32 s6, s10, s6
	s_mov_b32 s10, 35
	s_addc_u32 s7, s11, s7
	s_ashr_i32 s11, s10, 31
	s_lshl_b64 s[10:11], s[10:11], 3
	s_add_u32 s10, s0, s10
	s_addc_u32 s11, s1, s11
	s_load_dwordx2 s[10:11], s[10:11], 0x0
	s_waitcnt lgkmcnt(0)
	s_add_u32 s10, s10, s18
	s_addc_u32 s11, s11, s19
	s_add_u32 s10, s10, 0x12800000
	s_addc_u32 s11, s11, 0
	s_mov_b64 s[18:19], 0

.LBB0_922:
	s_andn2_b64 vcc, exec, s[54:55]
	s_mov_b32 s43, 0
	s_cbranch_vccnz .LBB0_924
	s_and_b64 s[6:7], s[4:5], exec
	s_movk_i32 s6, 0xa
	s_cselect_b32 s6, s6, 0xde5
	v_readlane_b32 s7, v254, 41
	s_add_i32 s43, s6, s7
